# baseline (speedup 1.0000x reference)
.LBB2_1:
	s_mov_b32 s17, s31
	s_mov_b32 s18, s15
	v_add_u32_e32 v196, s18, v192
	ds_read_b64_tr_b16 v[176:177], v196 offset:24576
	ds_read_b64_tr_b16 v[178:179], v196 offset:25088
	v_mfma_f32_32x32x16_f16 v[96:111], v[172:175], v[136:139], v[0:15]
	v_add_f32_e32 v80, v64, v65
	v_add_f32_e32 v80, v66, v80
	v_add_f32_e32 v80, v67, v80
	v_add_f32_e32 v80, v68, v80
	v_add_f32_e32 v80, v69, v80
	v_cvt_pk_f16_f32 v140, v64, v65
	v_cvt_pk_f16_f32 v141, v66, v67
	ds_read_b64_tr_b16 v[172:173], v196 offset:28672
	ds_read_b64_tr_b16 v[174:175], v196 offset:29184
	v_add_f32_e32 v64, v70, v80
	v_mfma_f32_32x32x16_f16 v[80:95], v[168:171], v[136:139], v[0:15]
	v_add_f32_e32 v64, v71, v64
	v_add_f32_e32 v64, v72, v64
	v_add_f32_e32 v64, v73, v64
	v_cvt_pk_f16_f32 v142, v68, v69
	v_cvt_pk_f16_f32 v143, v70, v71
	ds_read_b64_tr_b16 v[68:69], v196 offset:25600
	ds_read_b64_tr_b16 v[70:71], v196 offset:26112
	v_mfma_f32_32x32x16_f16 v[96:111], v[164:167], v[128:131], v[96:111]
	v_add_f32_e32 v64, v74, v64
	v_add_f32_e32 v64, v75, v64
	v_add_f32_e32 v64, v76, v64
	v_add_f32_e32 v116, v77, v64
	v_cvt_pk_f16_f32 v132, v72, v73
	v_cvt_pk_f16_f32 v133, v74, v75
	ds_read_b64_tr_b16 v[64:65], v196 offset:29696
	ds_read_b64_tr_b16 v[66:67], v196 offset:30208
	v_mfma_f32_32x32x16_f16 v[80:95], v[160:163], v[128:131], v[80:95]
	v_add_f32_e32 v72, v78, v116
	v_add_f32_e32 v72, v79, v72
	v_add_f32_e32 v72, v48, v72
	v_add_f32_e32 v116, v49, v72
	v_cvt_pk_f16_f32 v134, v76, v77
	v_cvt_pk_f16_f32 v135, v78, v79
	ds_read_b64_tr_b16 v[72:73], v196 offset:26624
	ds_read_b64_tr_b16 v[74:75], v196 offset:27136
	v_mfma_f32_32x32x16_f16 v[96:111], v[156:159], v[120:123], v[96:111]
	v_add_f32_e32 v76, v50, v116
	v_add_f32_e32 v76, v51, v76
	v_add_f32_e32 v76, v52, v76
	v_add_f32_e32 v76, v53, v76
	v_cvt_pk_f16_f32 v124, v48, v49
	v_cvt_pk_f16_f32 v125, v50, v51
	ds_read_b64_tr_b16 v[48:49], v196 offset:30720
	ds_read_b64_tr_b16 v[50:51], v196 offset:31232
	v_mfma_f32_32x32x16_f16 v[80:95], v[152:155], v[120:123], v[80:95]
	v_add_f32_e32 v76, v54, v76
	v_add_f32_e32 v76, v55, v76
	v_add_f32_e32 v76, v56, v76
	v_add_f32_e32 v76, v57, v76
	v_cvt_pk_f16_f32 v126, v52, v53
	v_cvt_pk_f16_f32 v127, v54, v55
	ds_read_b64_tr_b16 v[52:53], v196 offset:27648
	ds_read_b64_tr_b16 v[54:55], v196 offset:28160
	v_mfma_f32_32x32x16_f16 v[96:111], v[148:151], v[112:115], v[96:111]
	v_add_f32_e32 v76, v58, v76
	v_add_f32_e32 v76, v59, v76
	v_add_f32_e32 v76, v60, v76
	v_add_f32_e32 v76, v61, v76
	v_cvt_pk_f16_f32 v116, v56, v57
	v_cvt_pk_f16_f32 v117, v58, v59
	ds_read_b64_tr_b16 v[56:57], v196 offset:31744
	ds_read_b64_tr_b16 v[58:59], v196 offset:32256
	v_mfma_f32_32x32x16_f16 v[80:95], v[144:147], v[112:115], v[80:95]
	v_add_f32_e32 v76, v62, v76
	v_add_f32_e32 v76, v63, v76
	v_cvt_pk_f16_f32 v118, v60, v61
	v_cvt_pk_f16_f32 v119, v62, v63
	v_lshl_add_u64 v[60:61], v[182:183], 0, s[12:13]
	s_add_i32 m0, s14, s25
	v_cmp_lt_f32_e32 vcc, s36, v76
	global_load_lds_dwordx4 v[60:61], off
	s_add_i32 m0, s28, s26
	s_nop 0
	global_load_lds_dwordx4 v[180:181], off
	s_cbranch_vccnz .Lmy_rare_1

.LBB2_2:
	s_waitcnt lgkmcnt(8)
	v_mfma_f32_32x32x16_f16 v[16:31], v[140:143], v[176:179], v[16:31]
	v_exp_f32_e32 v96, v96
	v_exp_f32_e32 v97, v97
	v_exp_f32_e32 v98, v98
	v_exp_f32_e32 v99, v99
	v_mfma_f32_32x32x16_f16 v[32:47], v[140:143], v[172:175], v[32:47]
	v_exp_f32_e32 v100, v100
	v_exp_f32_e32 v101, v101
	v_exp_f32_e32 v102, v102
	v_exp_f32_e32 v103, v103
	v_add_u32_e32 v76, s19, v195
	ds_read_b128 v[60:63], v76
	ds_read_b128 v[148:151], v76 offset:512
	v_mfma_f32_32x32x16_f16 v[16:31], v[132:135], v[68:71], v[16:31]
	v_exp_f32_e32 v104, v104
	v_exp_f32_e32 v105, v105
	v_exp_f32_e32 v106, v106
	v_exp_f32_e32 v107, v107
	ds_read_b128 v[176:179], v76 offset:2048
	ds_read_b128 v[172:175], v76 offset:2560
	v_mfma_f32_32x32x16_f16 v[32:47], v[132:135], v[64:67], v[32:47]
	v_exp_f32_e32 v108, v108
	v_exp_f32_e32 v109, v109
	v_exp_f32_e32 v110, v110
	v_exp_f32_e32 v111, v111
	ds_read_b128 v[168:171], v76 offset:4096
	ds_read_b128 v[164:167], v76 offset:4608
	s_waitcnt lgkmcnt(6)
	v_mfma_f32_32x32x16_f16 v[16:31], v[124:127], v[72:75], v[16:31]
	v_exp_f32_e32 v80, v80
	v_exp_f32_e32 v81, v81
	v_exp_f32_e32 v82, v82
	v_exp_f32_e32 v83, v83
	ds_read_b128 v[160:163], v76 offset:6144
	ds_read_b128 v[156:159], v76 offset:6656
	v_mfma_f32_32x32x16_f16 v[32:47], v[124:127], v[48:51], v[32:47]
	v_exp_f32_e32 v84, v84
	v_exp_f32_e32 v85, v85
	v_exp_f32_e32 v86, v86
	v_exp_f32_e32 v87, v87
	v_mfma_f32_32x32x16_f16 v[16:31], v[116:119], v[52:55], v[16:31]
	v_exp_f32_e32 v88, v88
	v_exp_f32_e32 v89, v89
	v_exp_f32_e32 v90, v90
	v_exp_f32_e32 v91, v91
	v_mfma_f32_32x32x16_f16 v[32:47], v[116:119], v[56:59], v[32:47]
	v_exp_f32_e32 v92, v92
	v_exp_f32_e32 v93, v93
	v_exp_f32_e32 v94, v94
	v_exp_f32_e32 v95, v95
	s_waitcnt vmcnt(3) lgkmcnt(0)
	s_barrier
.LBB2_4:
	v_add_u32_e32 v196, s17, v192
	ds_read_b64_tr_b16 v[144:145], v196 offset:24576
	ds_read_b64_tr_b16 v[146:147], v196 offset:25088
	v_mfma_f32_32x32x16_f16 v[64:79], v[60:63], v[136:139], v[0:15]
	v_add_f32_e32 v48, v96, v97
	v_add_f32_e32 v48, v98, v48
	v_add_f32_e32 v48, v99, v48
	v_add_f32_e32 v48, v100, v48
	v_add_f32_e32 v48, v101, v48
	v_cvt_pk_f16_f32 v140, v96, v97
	v_cvt_pk_f16_f32 v141, v98, v99
	ds_read_b64_tr_b16 v[152:153], v196 offset:28672
	ds_read_b64_tr_b16 v[154:155], v196 offset:29184
	v_add_f32_e32 v48, v102, v48
	v_add_f32_e32 v48, v103, v48
	v_add_f32_e32 v48, v104, v48
	v_add_f32_e32 v96, v105, v48
	v_mfma_f32_32x32x16_f16 v[48:63], v[148:151], v[136:139], v[0:15]
	v_cvt_pk_f16_f32 v142, v100, v101
	v_cvt_pk_f16_f32 v143, v102, v103
	ds_read_b64_tr_b16 v[148:149], v196 offset:25600
	ds_read_b64_tr_b16 v[150:151], v196 offset:26112
	v_mfma_f32_32x32x16_f16 v[64:79], v[176:179], v[128:131], v[64:79]
	v_add_f32_e32 v96, v106, v96
	v_add_f32_e32 v96, v107, v96
	v_add_f32_e32 v96, v108, v96
	v_add_f32_e32 v96, v109, v96
	v_cvt_pk_f16_f32 v132, v104, v105
	v_cvt_pk_f16_f32 v133, v106, v107
	ds_read_b64_tr_b16 v[100:101], v196 offset:29696
	ds_read_b64_tr_b16 v[102:103], v196 offset:30208
	v_mfma_f32_32x32x16_f16 v[48:63], v[172:175], v[128:131], v[48:63]
	v_add_f32_e32 v96, v110, v96
	v_add_f32_e32 v96, v111, v96
	v_add_f32_e32 v96, v80, v96
	v_add_f32_e32 v104, v81, v96
	v_cvt_pk_f16_f32 v134, v108, v109
	v_cvt_pk_f16_f32 v135, v110, v111
	ds_read_b64_tr_b16 v[96:97], v196 offset:26624
	ds_read_b64_tr_b16 v[98:99], v196 offset:27136
	v_mfma_f32_32x32x16_f16 v[64:79], v[168:171], v[120:123], v[64:79]
	v_add_f32_e32 v104, v82, v104
	v_add_f32_e32 v104, v83, v104
	v_add_f32_e32 v104, v84, v104
	v_add_f32_e32 v104, v85, v104
	v_cvt_pk_f16_f32 v124, v80, v81
	v_cvt_pk_f16_f32 v125, v82, v83
	ds_read_b64_tr_b16 v[80:81], v196 offset:30720
	ds_read_b64_tr_b16 v[82:83], v196 offset:31232
	v_mfma_f32_32x32x16_f16 v[48:63], v[164:167], v[120:123], v[48:63]
	v_add_f32_e32 v104, v86, v104
	v_add_f32_e32 v104, v87, v104
	v_add_f32_e32 v104, v88, v104
	v_add_f32_e32 v104, v89, v104
	v_cvt_pk_f16_f32 v126, v84, v85
	v_cvt_pk_f16_f32 v127, v86, v87
	ds_read_b64_tr_b16 v[84:85], v196 offset:27648
	ds_read_b64_tr_b16 v[86:87], v196 offset:28160
	v_mfma_f32_32x32x16_f16 v[64:79], v[160:163], v[112:115], v[64:79]
	v_add_f32_e32 v104, v90, v104
	v_add_f32_e32 v104, v91, v104
	v_add_f32_e32 v104, v92, v104
	v_add_f32_e32 v104, v93, v104
	v_cvt_pk_f16_f32 v116, v88, v89
	v_cvt_pk_f16_f32 v117, v90, v91
	ds_read_b64_tr_b16 v[88:89], v196 offset:31744
	ds_read_b64_tr_b16 v[90:91], v196 offset:32256
	v_mfma_f32_32x32x16_f16 v[48:63], v[156:159], v[112:115], v[48:63]
	v_add_f32_e32 v104, v94, v104
	v_add_f32_e32 v104, v95, v104
	v_cvt_pk_f16_f32 v118, v92, v93
	v_cvt_pk_f16_f32 v119, v94, v95
	v_lshl_add_u64 v[92:93], v[182:183], 0, s[4:5]
	s_add_i32 m0, s19, s25
	v_cmp_lt_f32_e32 vcc, s36, v104
	global_load_lds_dwordx4 v[92:93], off
	s_add_i32 m0, s18, s26
	v_lshl_add_u64 v[92:93], v[184:185], 0, s[12:13]
	global_load_lds_dwordx4 v[92:93], off
	s_cbranch_vccnz .Lmy_rare_2

.LBB2_5:
	s_add_i32 s14, s19, 0x2000
	s_cmpk_lg_i32 s19, 0x4000
	s_cselect_b32 s14, s14, 0
	s_waitcnt lgkmcnt(8)
	v_mfma_f32_32x32x16_f16 v[16:31], v[140:143], v[144:147], v[16:31]
	v_exp_f32_e32 v64, v64
	v_exp_f32_e32 v65, v65
	v_exp_f32_e32 v66, v66
	v_exp_f32_e32 v67, v67
	v_mfma_f32_32x32x16_f16 v[32:47], v[140:143], v[152:155], v[32:47]
	v_exp_f32_e32 v68, v68
	v_exp_f32_e32 v69, v69
	v_exp_f32_e32 v70, v70
	v_exp_f32_e32 v71, v71
	v_add_u32_e32 v92, s14, v195
	ds_read_b128 v[172:175], v92
	ds_read_b128 v[168:171], v92 offset:512
	v_mfma_f32_32x32x16_f16 v[16:31], v[132:135], v[148:151], v[16:31]
	v_exp_f32_e32 v72, v72
	v_exp_f32_e32 v73, v73
	v_exp_f32_e32 v74, v74
	v_exp_f32_e32 v75, v75
	ds_read_b128 v[164:167], v92 offset:2048
	ds_read_b128 v[160:163], v92 offset:2560
	v_mfma_f32_32x32x16_f16 v[32:47], v[132:135], v[100:103], v[32:47]
	v_exp_f32_e32 v76, v76
	v_exp_f32_e32 v77, v77
	v_exp_f32_e32 v78, v78
	v_exp_f32_e32 v79, v79
	ds_read_b128 v[156:159], v92 offset:4096
	ds_read_b128 v[152:155], v92 offset:4608
	s_waitcnt lgkmcnt(6)
	v_mfma_f32_32x32x16_f16 v[16:31], v[124:127], v[96:99], v[16:31]
	v_exp_f32_e32 v48, v48
	v_exp_f32_e32 v49, v49
	v_exp_f32_e32 v50, v50
	v_exp_f32_e32 v51, v51
	ds_read_b128 v[148:151], v92 offset:6144
	ds_read_b128 v[144:147], v92 offset:6656
	v_mfma_f32_32x32x16_f16 v[32:47], v[124:127], v[80:83], v[32:47]
	v_exp_f32_e32 v52, v52
	v_exp_f32_e32 v53, v53
	v_exp_f32_e32 v54, v54
	v_exp_f32_e32 v55, v55
	v_mfma_f32_32x32x16_f16 v[16:31], v[116:119], v[84:87], v[16:31]
	v_exp_f32_e32 v56, v56
	v_exp_f32_e32 v57, v57
	v_exp_f32_e32 v58, v58
	v_exp_f32_e32 v59, v59
	v_mfma_f32_32x32x16_f16 v[32:47], v[116:119], v[88:91], v[32:47]
	v_exp_f32_e32 v60, v60
	v_exp_f32_e32 v61, v61
	v_exp_f32_e32 v62, v62
	v_exp_f32_e32 v63, v63
	s_add_i32 s6, s14, 0x2000
	s_cmpk_lg_i32 s14, 0x4000
	s_cselect_b32 s19, s6, 0
	s_add_i32 s27, s27, 2
	v_lshl_add_u64 v[180:181], v[180:181], 0, s[2:3]
	v_lshl_add_u64 v[182:183], v[182:183], 0, s[2:3]
	v_lshl_add_u64 v[184:185], v[184:185], 0, s[2:3]
	s_mov_b32 s15, s29
	s_mov_b32 s31, s28
	s_mov_b32 s29, s18
	s_mov_b32 s28, s17
	s_cmp_gt_u32 s27, 28
	s_waitcnt vmcnt(3) lgkmcnt(0)
	s_barrier
	s_cbranch_scc0 .LBB2_1
.LBB2_15:
	ds_read_b64_tr_b16 v[96:97], v192 offset:40960
	ds_read_b64_tr_b16 v[98:99], v192 offset:41472
	v_add_f32_e32 v80, v64, v65
	v_add_f32_e32 v80, v66, v80
	v_add_f32_e32 v80, v67, v80
	v_add_f32_e32 v80, v68, v80
	v_add_f32_e32 v100, v69, v80
	v_mfma_f32_32x32x16_f16 v[80:95], v[172:175], v[136:139], v[0:15]
	v_cvt_pk_f16_f32 v140, v64, v65
	v_cvt_pk_f16_f32 v141, v66, v67
	ds_read_b64_tr_b16 v[64:65], v192 offset:45056
	ds_read_b64_tr_b16 v[66:67], v192 offset:45568
	v_mfma_f32_32x32x16_f16 v[0:15], v[168:171], v[136:139], v[0:15]
	v_add_f32_e32 v100, v70, v100
	v_add_f32_e32 v100, v71, v100
	v_add_f32_e32 v100, v72, v100
	v_add_f32_e32 v100, v73, v100
	v_cvt_pk_f16_f32 v142, v68, v69
	v_cvt_pk_f16_f32 v143, v70, v71
	ds_read_b64_tr_b16 v[68:69], v192 offset:41984
	ds_read_b64_tr_b16 v[70:71], v192 offset:42496
	v_mfma_f32_32x32x16_f16 v[80:95], v[164:167], v[128:131], v[80:95]
	v_add_f32_e32 v100, v74, v100
	v_add_f32_e32 v100, v75, v100
	v_add_f32_e32 v100, v76, v100
	v_add_f32_e32 v100, v77, v100
	v_cvt_pk_f16_f32 v132, v72, v73
	v_cvt_pk_f16_f32 v133, v74, v75
	ds_read_b64_tr_b16 v[72:73], v192 offset:46080
	ds_read_b64_tr_b16 v[74:75], v192 offset:46592
	v_mfma_f32_32x32x16_f16 v[0:15], v[160:163], v[128:131], v[0:15]
	v_add_f32_e32 v100, v78, v100
	v_add_f32_e32 v100, v79, v100
	v_add_f32_e32 v100, v48, v100
	v_add_f32_e32 v100, v49, v100
	v_cvt_pk_f16_f32 v134, v76, v77
	v_cvt_pk_f16_f32 v135, v78, v79
	ds_read_b64_tr_b16 v[76:77], v192 offset:43008
	ds_read_b64_tr_b16 v[78:79], v192 offset:43520
	v_mfma_f32_32x32x16_f16 v[80:95], v[156:159], v[120:123], v[80:95]
	v_add_f32_e32 v100, v50, v100
	v_add_f32_e32 v100, v51, v100
	v_add_f32_e32 v100, v52, v100
	v_add_f32_e32 v104, v53, v100
	v_cvt_pk_f16_f32 v124, v48, v49
	v_cvt_pk_f16_f32 v125, v50, v51
	ds_read_b64_tr_b16 v[100:101], v192 offset:47104
	ds_read_b64_tr_b16 v[102:103], v192 offset:47616
	v_mfma_f32_32x32x16_f16 v[0:15], v[152:155], v[120:123], v[0:15]
	v_add_f32_e32 v48, v54, v104
	v_add_f32_e32 v48, v55, v48
	v_add_f32_e32 v48, v56, v48
	v_add_f32_e32 v48, v57, v48
	v_cvt_pk_f16_f32 v126, v52, v53
	v_cvt_pk_f16_f32 v127, v54, v55
	ds_read_b64_tr_b16 v[104:105], v192 offset:44032
	ds_read_b64_tr_b16 v[106:107], v192 offset:44544
	v_mfma_f32_32x32x16_f16 v[80:95], v[148:151], v[112:115], v[80:95]
	v_add_f32_e32 v48, v58, v48
	v_add_f32_e32 v48, v59, v48
	v_add_f32_e32 v48, v60, v48
	v_add_f32_e32 v48, v61, v48
	v_cvt_pk_f16_f32 v116, v56, v57
	v_cvt_pk_f16_f32 v117, v58, v59
	ds_read_b64_tr_b16 v[108:109], v192 offset:48128
	ds_read_b64_tr_b16 v[110:111], v192 offset:48640
	v_mfma_f32_32x32x16_f16 v[0:15], v[144:147], v[112:115], v[0:15]
	v_add_f32_e32 v48, v62, v48
	v_add_f32_e32 v48, v63, v48
	v_cvt_pk_f16_f32 v118, v60, v61
	v_cvt_pk_f16_f32 v119, v62, v63
	s_nop 0
	v_cmp_lt_f32_e32 vcc, s36, v48
	s_nop 4
	s_cbranch_vccnz .Lmy_rare_3

.LBB2_16:
	s_waitcnt lgkmcnt(8)
	v_mfma_f32_32x32x16_f16 v[16:31], v[140:143], v[96:99], v[16:31]
	v_exp_f32_e32 v80, v80
	v_exp_f32_e32 v81, v81
	v_exp_f32_e32 v82, v82
	v_exp_f32_e32 v83, v83
	v_mfma_f32_32x32x16_f16 v[32:47], v[140:143], v[64:67], v[32:47]
	v_exp_f32_e32 v84, v84
	v_exp_f32_e32 v85, v85
	v_exp_f32_e32 v86, v86
	v_exp_f32_e32 v87, v87
	v_mfma_f32_32x32x16_f16 v[16:31], v[132:135], v[68:71], v[16:31]
	v_exp_f32_e32 v88, v88
	v_exp_f32_e32 v89, v89
	v_exp_f32_e32 v90, v90
	v_exp_f32_e32 v91, v91
	v_mfma_f32_32x32x16_f16 v[32:47], v[132:135], v[72:75], v[32:47]
	v_exp_f32_e32 v92, v92
	v_exp_f32_e32 v93, v93
	v_exp_f32_e32 v94, v94
	v_exp_f32_e32 v95, v95
	s_waitcnt lgkmcnt(0)
	v_mfma_f32_32x32x16_f16 v[16:31], v[124:127], v[76:79], v[16:31]
	v_exp_f32_e32 v0, v0
	v_exp_f32_e32 v1, v1
	v_exp_f32_e32 v2, v2
	v_exp_f32_e32 v3, v3
	v_mfma_f32_32x32x16_f16 v[32:47], v[124:127], v[100:103], v[32:47]
	v_exp_f32_e32 v4, v4
	v_exp_f32_e32 v5, v5
	v_exp_f32_e32 v6, v6
	v_exp_f32_e32 v7, v7
	v_mfma_f32_32x32x16_f16 v[16:31], v[116:119], v[104:107], v[16:31]
	v_exp_f32_e32 v8, v8
	v_exp_f32_e32 v9, v9
	v_exp_f32_e32 v10, v10
	v_exp_f32_e32 v11, v11
	v_mfma_f32_32x32x16_f16 v[32:47], v[116:119], v[108:111], v[32:47]
	v_exp_f32_e32 v12, v12
	v_exp_f32_e32 v13, v13
	v_exp_f32_e32 v14, v14
	v_exp_f32_e32 v15, v15
	v_add_u32_e32 v48, s11, v193
